# speedup vs baseline: 1.0015x; 1.0015x over previous
_Z4k_lnPKDF16_PKfS2_PfPDF16_Phi:
	s_load_dword s3, s[0:1], 0x30
	s_and_b32 s4, s2, 7
	s_lshr_b32 s2, s2, 3
	v_lshrrev_b32_e32 v1, 6, v0
	s_waitcnt lgkmcnt(0)
	s_ashr_i32 s5, s3, 31
	s_lshr_b32 s5, s5, 27
	s_add_i32 s5, s3, s5
	s_ashr_i32 s5, s5, 5
	s_mul_i32 s4, s5, s4
	s_add_i32 s4, s4, s2
	v_lshl_or_b32 v2, s4, 2, v1
	v_cmp_gt_i32_e32 vcc, s3, v2
	s_and_saveexec_b64 s[2:3], vcc
	s_cbranch_execz .LBB1_13
	s_load_dwordx8 s[4:11], s[0:1], 0x0
	v_ashrrev_i32_e32 v3, 31, v2
	v_lshlrev_b32_e32 v4, 3, v0
	v_lshlrev_b64 v[0:1], 11, v[2:3]
	v_and_b32_e32 v8, 0x1f8, v4
	s_waitcnt lgkmcnt(0)
	v_lshl_add_u64 v[0:1], s[4:5], 0, v[0:1]
	v_mov_b32_e32 v11, 0
	v_lshlrev_b32_e32 v10, 1, v8
	v_lshl_add_u64 v[0:1], v[0:1], 0, v[10:11]
	global_load_dwordx4 v[4:7], v[0:1], off offset:1024 nt
	global_load_dwordx4 v[12:15], v[0:1], off nt
	v_mbcnt_lo_u32_b32 v0, -1, 0
	v_mbcnt_hi_u32_b32 v9, -1, v0
	v_and_b32_e32 v0, 64, v9
	v_xor_b32_e32 v1, 32, v9
	v_add_u32_e32 v22, 64, v0
	v_cmp_lt_i32_e32 vcc, v1, v22
	v_xor_b32_e32 v10, 16, v9
	s_load_dwordx2 s[4:5], s[0:1], 0x20
	v_cndmask_b32_e32 v0, v9, v1, vcc
	v_lshlrev_b32_e32 v54, 2, v0
	v_cmp_lt_i32_e32 vcc, v10, v22
	s_cmp_lg_u64 s[10:11], 0
	s_cselect_b64 s[2:3], -1, 0
	s_cmp_eq_u64 s[10:11], 0
	s_waitcnt vmcnt(1)
	v_cvt_f32_f16_e32 v20, v4
	s_waitcnt vmcnt(0)
	v_cvt_f32_f16_e32 v28, v14
	v_cvt_f32_f16_sdwa v29, v14 dst_sel:DWORD dst_unused:UNUSED_PAD src0_sel:WORD_1
	v_cvt_f32_f16_e32 v14, v12
	v_cvt_f32_f16_e32 v26, v15
	v_cvt_f32_f16_sdwa v27, v15 dst_sel:DWORD dst_unused:UNUSED_PAD src0_sel:WORD_1
	v_cvt_f32_f16_sdwa v15, v12 dst_sel:DWORD dst_unused:UNUSED_PAD src0_sel:WORD_1
	v_cvt_f32_f16_e32 v12, v13
	v_cvt_f32_f16_sdwa v13, v13 dst_sel:DWORD dst_unused:UNUSED_PAD src0_sel:WORD_1
	v_cvt_f32_f16_sdwa v21, v4 dst_sel:DWORD dst_unused:UNUSED_PAD src0_sel:WORD_1
	v_add_f32_e32 v4, 0, v14
	v_add_f32_e32 v4, v4, v15
	v_add_f32_e32 v4, v4, v12
	v_add_f32_e32 v4, v4, v13
	v_add_f32_e32 v4, v4, v28
	v_add_f32_e32 v4, v4, v29
	v_cvt_f32_f16_e32 v18, v5
	v_add_f32_e32 v4, v4, v26
	v_cvt_f32_f16_sdwa v19, v5 dst_sel:DWORD dst_unused:UNUSED_PAD src0_sel:WORD_1
	v_add_f32_e32 v4, v4, v27
	v_cvt_f32_f16_e32 v16, v6
	v_add_f32_e32 v4, v4, v20
	v_cvt_f32_f16_sdwa v17, v6 dst_sel:DWORD dst_unused:UNUSED_PAD src0_sel:WORD_1
	v_add_f32_e32 v4, v4, v21
	v_cvt_f32_f16_e32 v0, v7
	v_add_f32_e32 v4, v4, v18
	v_cvt_f32_f16_sdwa v1, v7 dst_sel:DWORD dst_unused:UNUSED_PAD src0_sel:WORD_1
	v_add_f32_e32 v4, v4, v19
	v_add_f32_e32 v4, v4, v16
	v_add_f32_e32 v4, v4, v17
	v_add_f32_e32 v4, v4, v0
	v_add_f32_e32 v4, v4, v1
	v_cndmask_b32_e32 v7, v9, v10, vcc
	v_lshlrev_b32_e32 v55, 2, v7
	v_xor_b32_e32 v6, 8, v9
	v_cmp_lt_i32_e32 vcc, v6, v22
	s_waitcnt lgkmcnt(0)
	v_mov_b32_e32 v5, v4
	s_nop 1
	v_permlane32_swap_b32_e32 v4, v5
	v_add_f32_e32 v4, v4, v5
	v_cndmask_b32_e32 v6, v9, v6, vcc
	v_lshlrev_b32_e32 v56, 2, v6
	v_xor_b32_e32 v7, 4, v9
	v_cmp_lt_i32_e32 vcc, v7, v22
	s_waitcnt lgkmcnt(0)
	v_mov_b32_e32 v5, v4
	s_nop 1
	v_permlane16_swap_b32_e32 v4, v5
	v_add_f32_e32 v4, v4, v5
	v_cndmask_b32_e32 v7, v9, v7, vcc
	v_lshlrev_b32_e32 v57, 2, v7
	v_xor_b32_e32 v6, 2, v9
	v_cmp_lt_i32_e32 vcc, v6, v22
	s_waitcnt lgkmcnt(0)
	s_nop 1
	v_add_f32_dpp v4, v4, v4 row_ror:8 row_mask:0xf bank_mask:0xf
	v_cndmask_b32_e32 v6, v9, v6, vcc
	v_lshlrev_b32_e32 v58, 2, v6
	v_xor_b32_e32 v7, 1, v9
	v_cmp_lt_i32_e32 vcc, v7, v22
	s_waitcnt lgkmcnt(0)
	s_nop 1
	v_add_f32_dpp v4, v4, v4 row_ror:4 row_mask:0xf bank_mask:0xf
	v_cndmask_b32_e32 v6, v9, v7, vcc
	v_lshlrev_b32_e32 v10, 2, v8
	v_lshlrev_b32_e32 v9, 2, v6
	s_waitcnt lgkmcnt(0)
	s_nop 1
	v_add_f32_dpp v30, v4, v4 row_ror:2 row_mask:0xf bank_mask:0xf
	global_load_dwordx4 v[4:7], v10, s[6:7]
	global_load_dwordx4 v[22:25], v10, s[8:9]
	global_load_dwordx4 v[32:35], v10, s[6:7] offset:16
	global_load_dwordx4 v[36:39], v10, s[8:9] offset:16
	s_waitcnt lgkmcnt(0)
	s_nop 1
	v_add_f32_dpp v30, v30, v30 row_ror:1 row_mask:0xf bank_mask:0xf
	v_mul_f32_e32 v30, 0x3a800000, v30
	v_pk_add_f32 v[40:41], v[14:15], v[30:31] op_sel_hi:[1,0] neg_lo:[0,1] neg_hi:[0,1]
	v_pk_add_f32 v[42:43], v[12:13], v[30:31] op_sel_hi:[1,0] neg_lo:[0,1] neg_hi:[0,1]
	v_pk_add_f32 v[12:13], v[18:19], v[30:31] op_sel_hi:[1,0] neg_lo:[0,1] neg_hi:[0,1]
	v_pk_add_f32 v[18:19], v[16:17], v[30:31] op_sel_hi:[1,0] neg_lo:[0,1] neg_hi:[0,1]
	v_pk_add_f32 v[16:17], v[0:1], v[30:31] op_sel_hi:[1,0] neg_lo:[0,1] neg_hi:[0,1]
	v_pk_mul_f32 v[0:1], v[40:41], v[40:41]
	v_pk_add_f32 v[14:15], v[20:21], v[30:31] op_sel_hi:[1,0] neg_lo:[0,1] neg_hi:[0,1]
	v_pk_mul_f32 v[20:21], v[42:43], v[42:43]
	v_add_f32_e32 v0, v0, v1
	v_pk_add_f32 v[44:45], v[28:29], v[30:31] op_sel_hi:[1,0] neg_lo:[0,1] neg_hi:[0,1]
	v_add_f32_e32 v0, v0, v20
	v_pk_mul_f32 v[28:29], v[44:45], v[44:45]
	v_add_f32_e32 v0, v0, v21
	v_pk_add_f32 v[26:27], v[26:27], v[30:31] op_sel_hi:[1,0] neg_lo:[0,1] neg_hi:[0,1]
	v_add_f32_e32 v0, v0, v28
	v_pk_mul_f32 v[30:31], v[26:27], v[26:27]
	v_add_f32_e32 v0, v0, v29
	v_add_f32_e32 v0, v0, v30
	v_pk_mul_f32 v[46:47], v[14:15], v[14:15]
	v_add_f32_e32 v0, v0, v31
	v_add_f32_e32 v0, v0, v46
	v_pk_mul_f32 v[48:49], v[12:13], v[12:13]
	v_add_f32_e32 v0, v0, v47
	v_add_f32_e32 v0, v0, v48
	v_pk_mul_f32 v[50:51], v[18:19], v[18:19]
	v_add_f32_e32 v0, v0, v49
	v_add_f32_e32 v0, v0, v50
	v_pk_mul_f32 v[52:53], v[16:17], v[16:17]
	v_add_f32_e32 v0, v0, v51
	v_add_f32_e32 v0, v0, v52
	v_add_f32_e32 v0, v0, v53
	v_mov_b32_e32 v20, 0x3727c5ac
	v_lshlrev_b64 v[30:31], 10, v[2:3]
	s_waitcnt lgkmcnt(0)
	v_mov_b32_e32 v1, v0
	s_nop 1
	v_permlane32_swap_b32_e32 v0, v1
	v_add_f32_e32 v0, v0, v1
	s_waitcnt lgkmcnt(0)
	v_mov_b32_e32 v1, v0
	s_nop 1
	v_permlane16_swap_b32_e32 v0, v1
	v_add_f32_e32 v0, v0, v1
	s_waitcnt lgkmcnt(0)
	s_nop 1
	v_add_f32_dpp v0, v0, v0 row_ror:8 row_mask:0xf bank_mask:0xf
	s_waitcnt lgkmcnt(0)
	s_nop 1
	v_add_f32_dpp v0, v0, v0 row_ror:4 row_mask:0xf bank_mask:0xf
	s_waitcnt lgkmcnt(0)
	s_nop 1
	v_add_f32_dpp v21, v0, v0 row_ror:2 row_mask:0xf bank_mask:0xf
	v_lshlrev_b64 v[0:1], 12, v[2:3]
	v_mov_b32_e32 v9, v11
	s_waitcnt lgkmcnt(0)
	s_nop 1
	v_add_f32_dpp v2, v21, v21 row_ror:1 row_mask:0xf bank_mask:0xf
	v_fmac_f32_e32 v20, 0x3a800000, v2
	v_rsq_f32_e32 v28, v20
	v_lshl_add_u64 v[20:21], s[10:11], 0, v[0:1]
	v_pk_mul_f32 v[0:1], v[28:29], v[40:41] op_sel_hi:[0,1]
	v_pk_mul_f32 v[2:3], v[28:29], v[44:45] op_sel_hi:[0,1]
	v_pk_mul_f32 v[40:41], v[28:29], v[42:43] op_sel_hi:[0,1]
	v_pk_mul_f32 v[26:27], v[28:29], v[26:27] op_sel_hi:[0,1]
	s_waitcnt vmcnt(2)
	v_pk_fma_f32 v[4:5], v[4:5], v[0:1], v[22:23]
	s_waitcnt vmcnt(0)
	v_pk_fma_f32 v[0:1], v[32:33], v[2:3], v[36:37]
	v_pk_fma_f32 v[6:7], v[6:7], v[40:41], v[24:25]
	v_pk_fma_f32 v[2:3], v[34:35], v[26:27], v[38:39]
	v_lshlrev_b32_e32 v26, 2, v8
	s_cbranch_scc1 .LBB1_3
	v_mov_b32_e32 v27, v11
	v_lshl_add_u64 v[22:23], v[20:21], 0, v[26:27]
	global_store_dwordx4 v[22:23], v[4:7], off nt
	global_store_dwordx4 v[22:23], v[0:3], off offset:16 nt
